# pool/head-norm phase: per-head sums of squares by DPP row-rotate adds instead of 16 ds_bpermute round trips
# baseline (speedup 1.0000x reference)
; __device__ __forceinline__ float bflo(unsigned w) { return __uint_as_float(w << 16); }
; __device__ __forceinline__ float bfhi(unsigned w) { return __uint_as_float(w & 0xffff0000u); }
; __device__ __forceinline__ void p5_pool_yb(const Args& a, const Frame& F) {
;     ...
;     for (int t0 = gw * 4; t0 < T; t0 += NGW * 4) {
;         u32x4 f[4], bk[4], og[4];
; #pragma unroll
;         for (int u = 0; u < 4; ++u) { const size_t o = (size_t)(t0 + u) * 512 + F.lane * 8; f[u] = *(const u32x4*)(HF + o); bk[u] = *(const u32x4*)(HB + o); og[u] = *(const u32x4*)(POg + o); }
; #pragma unroll
;         for (int u = 0; u < 4; ++u) {
;             float v[8];
;             v[0] = bflo(f[u].x) + bflo(bk[u].x); v[1] = bfhi(f[u].x) + bfhi(bk[u].x); v[2] = bflo(f[u].y) + bflo(bk[u].y); v[3] = bfhi(f[u].y) + bfhi(bk[u].y);
;             v[4] = bflo(f[u].z) + bflo(bk[u].z); v[5] = bfhi(f[u].z) + bfhi(bk[u].z); v[6] = bflo(f[u].w) + bflo(bk[u].w); v[7] = bfhi(f[u].w) + bfhi(bk[u].w);
;             float s2 = 0.f;
; #pragma unroll
;             for (int jj = 0; jj < 8; ++jj) s2 += v[jj] * v[jj];
.LBB0_579:
	v_add_co_u32_e32 v30, vcc, 0xefa00000, v26
	global_load_dwordx4 v[22:25], v[26:27], off offset:-3072 nt
	global_load_dwordx4 v[18:21], v[26:27], off offset:-2048 nt
	global_load_dwordx4 v[14:17], v[26:27], off offset:-1024 nt
	global_load_dwordx4 v[10:13], v[26:27], off nt
	v_addc_co_u32_e32 v31, vcc, -1, v27, vcc
	v_add_co_u32_e32 v68, vcc, 0xf3a00000, v26
	global_load_dwordx4 v[36:39], v[30:31], off offset:-3072 nt
	s_nop 0
	v_addc_co_u32_e32 v69, vcc, -1, v27, vcc
	global_load_dwordx4 v[40:43], v[30:31], off offset:-2048 nt
	global_load_dwordx4 v[44:47], v[30:31], off offset:-1024 nt
	global_load_dwordx4 v[48:51], v[30:31], off nt
	global_load_dwordx4 v[52:55], v[68:69], off offset:-3072 nt
	global_load_dwordx4 v[56:59], v[68:69], off offset:-2048 nt
	global_load_dwordx4 v[60:63], v[68:69], off offset:-1024 nt
	global_load_dwordx4 v[64:67], v[68:69], off nt
	v_add_co_u32_e64 v28, s[0:1], s13, v26
	s_add_i32 s10, s10, s12
	s_nop 0
	v_addc_co_u32_e64 v29, s[0:1], -1, v27, s[0:1]
	s_cmp_lt_i32 s10, 0x10000
	v_lshl_add_u64 v[26:27], v[26:27], 0, s[14:15]
	s_waitcnt vmcnt(0)
	v_lshlrev_b32_e32 v30, 16, v22
	v_and_b32_e32 v22, 0xffff0000, v22
	v_lshlrev_b32_e32 v31, 16, v23
	v_and_b32_e32 v23, 0xffff0000, v23
	v_lshlrev_b32_e32 v68, 16, v24
	v_and_b32_e32 v24, 0xffff0000, v24
	v_lshlrev_b32_e32 v69, 16, v25
	v_and_b32_e32 v25, 0xffff0000, v25
	v_lshlrev_b32_e32 v70, 16, v18
	v_and_b32_e32 v18, 0xffff0000, v18
	v_lshlrev_b32_e32 v71, 16, v19
	v_and_b32_e32 v19, 0xffff0000, v19
	v_lshlrev_b32_e32 v72, 16, v20
	v_and_b32_e32 v20, 0xffff0000, v20
	v_lshlrev_b32_e32 v73, 16, v21
	v_and_b32_e32 v21, 0xffff0000, v21
	v_lshlrev_b32_e32 v74, 16, v14
	v_and_b32_e32 v14, 0xffff0000, v14
	v_lshlrev_b32_e32 v75, 16, v15
	v_and_b32_e32 v15, 0xffff0000, v15
	v_lshlrev_b32_e32 v76, 16, v16
	v_and_b32_e32 v16, 0xffff0000, v16
	v_lshlrev_b32_e32 v77, 16, v17
	v_and_b32_e32 v17, 0xffff0000, v17
	v_lshlrev_b32_e32 v78, 16, v10
	v_and_b32_e32 v10, 0xffff0000, v10
	v_lshlrev_b32_e32 v79, 16, v11
	v_and_b32_e32 v11, 0xffff0000, v11
	v_lshlrev_b32_e32 v80, 16, v12
	v_and_b32_e32 v12, 0xffff0000, v12
	v_lshlrev_b32_e32 v81, 16, v13
	v_and_b32_e32 v13, 0xffff0000, v13
	v_lshlrev_b32_e32 v94, 16, v36
	v_lshlrev_b32_e32 v108, 16, v52
	v_mul_f32_e32 v30, 0xbfb8aa3b, v30
	v_mul_f32_e32 v22, 0xbfb8aa3b, v22
	v_mul_f32_e32 v31, 0xbfb8aa3b, v31
	v_mul_f32_e32 v23, 0xbfb8aa3b, v23
	v_mul_f32_e32 v24, 0xbfb8aa3b, v24
	v_mul_f32_e32 v25, 0xbfb8aa3b, v25
	v_mul_f32_e32 v82, 0xbfb8aa3b, v18
	v_mul_f32_e32 v83, 0xbfb8aa3b, v19
	v_mul_f32_e32 v84, 0xbfb8aa3b, v20
	v_mul_f32_e32 v85, 0xbfb8aa3b, v21
	v_mul_f32_e32 v86, 0xbfb8aa3b, v14
	v_mul_f32_e32 v87, 0xbfb8aa3b, v15
	v_mul_f32_e32 v88, 0xbfb8aa3b, v16
	v_mul_f32_e32 v89, 0xbfb8aa3b, v17
	v_mul_f32_e32 v90, 0xbfb8aa3b, v10
	v_mul_f32_e32 v91, 0xbfb8aa3b, v11
	v_mul_f32_e32 v92, 0xbfb8aa3b, v12
	v_mul_f32_e32 v93, 0xbfb8aa3b, v13
	v_and_b32_e32 v95, 0xffff0000, v36
	v_lshlrev_b32_e32 v11, 16, v37
	v_and_b32_e32 v10, 0xffff0000, v37
	v_lshlrev_b32_e32 v13, 16, v38
	v_and_b32_e32 v12, 0xffff0000, v38
	v_lshlrev_b32_e32 v15, 16, v39
	v_and_b32_e32 v14, 0xffff0000, v39
	v_lshlrev_b32_e32 v102, 16, v40
	v_and_b32_e32 v103, 0xffff0000, v40
	v_lshlrev_b32_e32 v17, 16, v41
	v_and_b32_e32 v16, 0xffff0000, v41
	v_lshlrev_b32_e32 v19, 16, v42
	v_and_b32_e32 v18, 0xffff0000, v42
	v_lshlrev_b32_e32 v21, 16, v43
	v_and_b32_e32 v20, 0xffff0000, v43
	v_lshlrev_b32_e32 v104, 16, v44
	v_lshlrev_b32_e32 v106, 16, v48
	v_and_b32_e32 v107, 0xffff0000, v48
	v_lshlrev_b32_e32 v37, 16, v49
	v_and_b32_e32 v36, 0xffff0000, v49
	v_lshlrev_b32_e32 v39, 16, v50
	v_and_b32_e32 v38, 0xffff0000, v50
	v_lshlrev_b32_e32 v41, 16, v51
	v_and_b32_e32 v40, 0xffff0000, v51
	v_and_b32_e32 v109, 0xffff0000, v52
	v_lshlrev_b32_e32 v43, 16, v53
	v_and_b32_e32 v42, 0xffff0000, v53
	v_lshlrev_b32_e32 v110, 16, v56
	v_and_b32_e32 v111, 0xffff0000, v56
	v_lshlrev_b32_e32 v49, 16, v57
	v_and_b32_e32 v48, 0xffff0000, v57
	v_lshlrev_b32_e32 v51, 16, v58
	v_and_b32_e32 v50, 0xffff0000, v58
	v_lshlrev_b32_e32 v53, 16, v59
	v_and_b32_e32 v52, 0xffff0000, v59
	v_lshlrev_b32_e32 v112, 16, v60
	v_lshlrev_b32_e32 v57, 16, v62
	v_and_b32_e32 v56, 0xffff0000, v62
	v_lshlrev_b32_e32 v59, 16, v63
	v_and_b32_e32 v58, 0xffff0000, v63
	v_lshlrev_b32_e32 v114, 16, v64
	v_lshlrev_b32_e32 v63, 16, v66
	v_and_b32_e32 v62, 0xffff0000, v66
	v_add_f32_e32 v66, v108, v94
	v_exp_f32_e32 v96, v30
	v_exp_f32_e32 v97, v22
	v_exp_f32_e32 v98, v31
	v_exp_f32_e32 v99, v23
	v_exp_f32_e32 v100, v24
	v_exp_f32_e32 v101, v25
	v_and_b32_e32 v105, 0xffff0000, v44
	v_lshlrev_b32_e32 v23, 16, v45
	v_and_b32_e32 v22, 0xffff0000, v45
	v_lshlrev_b32_e32 v25, 16, v46
	v_and_b32_e32 v24, 0xffff0000, v46
	v_lshlrev_b32_e32 v31, 16, v47
	v_and_b32_e32 v30, 0xffff0000, v47
	v_lshlrev_b32_e32 v45, 16, v54
	v_and_b32_e32 v44, 0xffff0000, v54
	v_lshlrev_b32_e32 v47, 16, v55
	v_and_b32_e32 v46, 0xffff0000, v55
	v_and_b32_e32 v113, 0xffff0000, v60
	v_lshlrev_b32_e32 v55, 16, v61
	v_and_b32_e32 v54, 0xffff0000, v61
	v_and_b32_e32 v115, 0xffff0000, v64
	v_lshlrev_b32_e32 v61, 16, v65
	v_and_b32_e32 v60, 0xffff0000, v65
	v_lshlrev_b32_e32 v65, 16, v67
	v_and_b32_e32 v64, 0xffff0000, v67
	v_add_f32_e32 v67, v109, v95
	v_pk_add_f32 v[10:11], v[10:11], v[42:43]
	v_add_f32_e32 v94, v110, v102
	v_add_f32_e32 v102, v112, v104
	v_add_f32_e32 v104, v114, v106
	v_mul_f32_e32 v106, v66, v66
	v_pk_mul_f32 v[42:43], v[10:11], v[10:11]
	v_fmac_f32_e32 v106, v67, v67
	v_pk_add_f32 v[12:13], v[12:13], v[44:45]
	v_add_f32_e32 v95, v111, v103
	v_pk_add_f32 v[16:17], v[16:17], v[48:49]
	v_add_f32_e32 v103, v113, v105
; __device__ __forceinline__ float bflo(unsigned w) { return __uint_as_float(w << 16); }
; __device__ __forceinline__ float bfhi(unsigned w) { return __uint_as_float(w & 0xffff0000u); }
; __device__ __forceinline__ float sigmoidf_(float x) { return frcp_(1.0f + fexp_(-x)); }
; __device__ __forceinline__ void p5_pool_yb(const Args& a, const Frame& F) {
;     ...
;             float s2 = 0.f;
; #pragma unroll
;             for (int jj = 0; jj < 8; ++jj) s2 += v[jj] * v[jj];
; #pragma unroll
;             for (int o = 1; o < 16; o <<= 1) s2 += __shfl_xor(s2, o);
;             const float rstd = rsqrtf(s2 * (1.f / 128.f) + EPS);
;             float gsig[8];
;             gsig[0] = sigmoidf_(bflo(og[u].x)); gsig[1] = sigmoidf_(bfhi(og[u].x)); gsig[2] = sigmoidf_(bflo(og[u].y)); gsig[3] = sigmoidf_(bfhi(og[u].y));
;             gsig[4] = sigmoidf_(bflo(og[u].z)); gsig[5] = sigmoidf_(bfhi(og[u].z)); gsig[6] = sigmoidf_(bflo(og[u].w)); gsig[7] = sigmoidf_(bfhi(og[u].w));
	v_pk_add_f32 v[22:23], v[22:23], v[54:55]
	v_add_f32_e32 v105, v115, v107
	v_pk_add_f32 v[36:37], v[36:37], v[60:61]
	v_mul_f32_e32 v107, v94, v94
	v_mul_f32_e32 v108, v102, v102
	v_mul_f32_e32 v109, v104, v104
	v_add_f32_e32 v43, v43, v106
	v_pk_mul_f32 v[44:45], v[12:13], v[12:13]
	v_pk_mul_f32 v[48:49], v[16:17], v[16:17]
	v_pk_mul_f32 v[54:55], v[22:23], v[22:23]
	v_pk_mul_f32 v[60:61], v[36:37], v[36:37]
	v_fmac_f32_e32 v107, v95, v95
	v_fmac_f32_e32 v108, v103, v103
	v_fmac_f32_e32 v109, v105, v105
	v_add_f32_e32 v42, v42, v43
	v_pk_add_f32 v[14:15], v[14:15], v[46:47]
	v_pk_add_f32 v[18:19], v[18:19], v[50:51]
	v_pk_add_f32 v[24:25], v[24:25], v[56:57]
	v_pk_add_f32 v[38:39], v[38:39], v[62:63]
	v_add_f32_e32 v49, v49, v107
	v_add_f32_e32 v55, v55, v108
	v_add_f32_e32 v61, v61, v109
	v_add_f32_e32 v42, v45, v42
	v_pk_mul_f32 v[46:47], v[14:15], v[14:15]
	v_pk_mul_f32 v[50:51], v[18:19], v[18:19]
	v_pk_mul_f32 v[56:57], v[24:25], v[24:25]
	v_pk_mul_f32 v[62:63], v[38:39], v[38:39]
	v_add_f32_e32 v43, v48, v49
	v_add_f32_e32 v48, v54, v55
	v_add_f32_e32 v49, v60, v61
	v_add_f32_e32 v42, v44, v42
	v_pk_add_f32 v[20:21], v[20:21], v[52:53]
	v_pk_add_f32 v[30:31], v[30:31], v[58:59]
	v_pk_add_f32 v[40:41], v[40:41], v[64:65]
	v_add_f32_e32 v43, v51, v43
	v_add_f32_e32 v45, v57, v48
	v_add_f32_e32 v48, v63, v49
	v_add_f32_e32 v42, v47, v42
	v_pk_mul_f32 v[52:53], v[20:21], v[20:21]
	v_pk_mul_f32 v[58:59], v[30:31], v[30:31]
	v_pk_mul_f32 v[64:65], v[40:41], v[40:41]
	v_add_f32_e32 v43, v50, v43
	v_add_f32_e32 v44, v56, v45
	v_add_f32_e32 v45, v62, v48
	v_add_f32_e32 v42, v46, v42
	v_add_f32_e32 v43, v53, v43
	v_add_f32_e32 v44, v59, v44
	v_add_f32_e32 v45, v65, v45
	v_add_f32_e32 v43, v52, v43
	v_add_f32_e32 v44, v58, v44
	v_add_f32_e32 v45, v64, v45
	s_nop 1
	v_add_f32_dpp v42, v42, v42 row_ror:8 row_mask:0xf bank_mask:0xf bound_ctrl:1
	v_add_f32_dpp v43, v43, v43 row_ror:8 row_mask:0xf bank_mask:0xf bound_ctrl:1
	v_add_f32_dpp v44, v44, v44 row_ror:8 row_mask:0xf bank_mask:0xf bound_ctrl:1
	v_add_f32_dpp v45, v45, v45 row_ror:8 row_mask:0xf bank_mask:0xf bound_ctrl:1
	v_add_f32_dpp v42, v42, v42 row_ror:4 row_mask:0xf bank_mask:0xf bound_ctrl:1
	v_add_f32_dpp v43, v43, v43 row_ror:4 row_mask:0xf bank_mask:0xf bound_ctrl:1
	v_add_f32_dpp v44, v44, v44 row_ror:4 row_mask:0xf bank_mask:0xf bound_ctrl:1
	v_add_f32_dpp v45, v45, v45 row_ror:4 row_mask:0xf bank_mask:0xf bound_ctrl:1
	v_add_f32_dpp v42, v42, v42 row_ror:2 row_mask:0xf bank_mask:0xf bound_ctrl:1
	v_add_f32_dpp v43, v43, v43 row_ror:2 row_mask:0xf bank_mask:0xf bound_ctrl:1
	v_add_f32_dpp v44, v44, v44 row_ror:2 row_mask:0xf bank_mask:0xf bound_ctrl:1
	v_add_f32_dpp v45, v45, v45 row_ror:2 row_mask:0xf bank_mask:0xf bound_ctrl:1
	v_add_f32_dpp v42, v42, v42 row_ror:1 row_mask:0xf bank_mask:0xf bound_ctrl:1
	v_add_f32_dpp v43, v43, v43 row_ror:1 row_mask:0xf bank_mask:0xf bound_ctrl:1
	v_add_f32_dpp v44, v44, v44 row_ror:1 row_mask:0xf bank_mask:0xf bound_ctrl:1
	v_add_f32_dpp v45, v45, v45 row_ror:1 row_mask:0xf bank_mask:0xf bound_ctrl:1
	v_fmamk_f32 v42, v42, 0x3c000000, v35
	v_mul_f32_e32 v68, 0xbfb8aa3b, v68
	v_mul_f32_e32 v46, 0x4b800000, v42
	v_cmp_gt_f32_e64 s[6:7], s11, v42
	v_mul_f32_e32 v69, 0xbfb8aa3b, v69
	v_exp_f32_e32 v68, v68
	v_fmamk_f32 v43, v43, 0x3c000000, v35
	v_fmamk_f32 v44, v44, 0x3c000000, v35
	v_fmamk_f32 v45, v45, 0x3c000000, v35
	v_cndmask_b32_e64 v42, v42, v46, s[6:7]
	v_mul_f32_e32 v70, 0xbfb8aa3b, v70
	v_mul_f32_e32 v71, 0xbfb8aa3b, v71
	v_mul_f32_e32 v72, 0xbfb8aa3b, v72
	v_mul_f32_e32 v73, 0xbfb8aa3b, v73
	v_exp_f32_e32 v69, v69
	v_mul_f32_e32 v47, 0x4b800000, v43
	v_cmp_gt_f32_e32 vcc, s11, v43
	v_mul_f32_e32 v48, 0x4b800000, v44
	v_cmp_gt_f32_e64 s[0:1], s11, v44
	v_mul_f32_e32 v49, 0x4b800000, v45
	v_cmp_gt_f32_e64 s[4:5], s11, v45
	v_rsq_f32_e32 v42, v42
	v_mul_f32_e32 v74, 0xbfb8aa3b, v74
	v_mul_f32_e32 v75, 0xbfb8aa3b, v75
	v_mul_f32_e32 v76, 0xbfb8aa3b, v76
	v_mul_f32_e32 v77, 0xbfb8aa3b, v77
	v_exp_f32_e32 v70, v70
	v_exp_f32_e32 v82, v82
	v_exp_f32_e32 v71, v71
	v_exp_f32_e32 v83, v83
	v_exp_f32_e32 v72, v72
	v_exp_f32_e32 v84, v84
	v_exp_f32_e32 v73, v73
	v_exp_f32_e32 v85, v85
	v_cndmask_b32_e32 v43, v43, v47, vcc
	v_cndmask_b32_e64 v44, v44, v48, s[0:1]
	v_cndmask_b32_e64 v45, v45, v49, s[4:5]
	v_mul_f32_e32 v78, 0xbfb8aa3b, v78
	v_mul_f32_e32 v79, 0xbfb8aa3b, v79
	v_mul_f32_e32 v80, 0xbfb8aa3b, v80
	v_mul_f32_e32 v81, 0xbfb8aa3b, v81
	v_exp_f32_e32 v74, v74
	v_exp_f32_e32 v86, v86
	v_exp_f32_e32 v75, v75
	v_exp_f32_e32 v87, v87
	v_exp_f32_e32 v76, v76
	v_exp_f32_e32 v88, v88
	v_exp_f32_e32 v77, v77
	v_exp_f32_e32 v89, v89
	v_rsq_f32_e32 v43, v43
	v_rsq_f32_e32 v44, v44
	v_rsq_f32_e32 v45, v45
	v_exp_f32_e32 v78, v78
	v_exp_f32_e32 v90, v90
	v_exp_f32_e32 v79, v79
	v_exp_f32_e32 v91, v91
	v_exp_f32_e32 v80, v80
	v_exp_f32_e32 v92, v92
	v_exp_f32_e32 v81, v81
	v_exp_f32_e32 v93, v93
	v_add_f32_e32 v98, 1.0, v98
	v_add_f32_e32 v68, 1.0, v68
	v_add_f32_e32 v100, 1.0, v100
	v_add_f32_e32 v96, 1.0, v96
	v_add_f32_e32 v97, 1.0, v97
	v_add_f32_e32 v99, 1.0, v99
	v_add_f32_e32 v69, 1.0, v69
	v_add_f32_e32 v101, 1.0, v101
	v_rcp_f32_e32 v98, v98
	v_rcp_f32_e32 v68, v68
	v_rcp_f32_e32 v100, v100
	v_mul_f32_e32 v46, 0x45800000, v42
; __device__ __forceinline__ float bflo(unsigned w) { return __uint_as_float(w << 16); }
; __device__ __forceinline__ float bfhi(unsigned w) { return __uint_as_float(w & 0xffff0000u); }
; __device__ __forceinline__ float sigmoidf_(float x) { return frcp_(1.0f + fexp_(-x)); }
; __device__ __forceinline__ unsigned cvt_pk_bf16(float lo, float hi) { unsigned r; asm volatile("v_cvt_pk_bf16_f32 %0, %1, %2" : "=v"(r) : "v"(lo), "v"(hi)); return r; }
; __device__ __forceinline__ void p5_pool_yb(const Args& a, const Frame& F) {
;     ...
;             const float rstd = rsqrtf(s2 * (1.f / 128.f) + EPS);
;             float gsig[8];
;             gsig[0] = sigmoidf_(bflo(og[u].x)); gsig[1] = sigmoidf_(bfhi(og[u].x)); gsig[2] = sigmoidf_(bflo(og[u].y)); gsig[3] = sigmoidf_(bfhi(og[u].y));
;             gsig[4] = sigmoidf_(bflo(og[u].z)); gsig[5] = sigmoidf_(bfhi(og[u].z)); gsig[6] = sigmoidf_(bflo(og[u].w)); gsig[7] = sigmoidf_(bfhi(og[u].w));
;             float r[8];
; #pragma unroll
;             for (int jj = 0; jj < 8; ++jj) r[jj] = v[jj] * rstd * hwv[jj] * gsig[jj];
;             u32x4 wv; wv.x = pg8::cvt_pk_bf16(r[0], r[1]); wv.y = pg8::cvt_pk_bf16(r[2], r[3]); wv.z = pg8::cvt_pk_bf16(r[4], r[5]); wv.w = pg8::cvt_pk_bf16(r[6], r[7]);
;             *(u32x4*)(YB + (size_t)(t0 + u) * 512 + F.lane * 8) = wv;
;         }
	v_add_f32_e32 v70, 1.0, v70
	v_add_f32_e32 v82, 1.0, v82
	v_add_f32_e32 v71, 1.0, v71
	v_add_f32_e32 v83, 1.0, v83
	v_add_f32_e32 v72, 1.0, v72
	v_add_f32_e32 v84, 1.0, v84
	v_add_f32_e32 v73, 1.0, v73
	v_add_f32_e32 v85, 1.0, v85
	v_rcp_f32_e32 v96, v96
	v_rcp_f32_e32 v97, v97
	v_rcp_f32_e32 v99, v99
	v_rcp_f32_e32 v69, v69
	v_rcp_f32_e32 v101, v101
	v_cndmask_b32_e64 v42, v42, v46, s[6:7]
	v_add_f32_e32 v74, 1.0, v74
	v_add_f32_e32 v86, 1.0, v86
	v_add_f32_e32 v75, 1.0, v75
	v_add_f32_e32 v87, 1.0, v87
	v_add_f32_e32 v76, 1.0, v76
	v_add_f32_e32 v88, 1.0, v88
	v_add_f32_e32 v77, 1.0, v77
	v_add_f32_e32 v89, 1.0, v89
	v_rcp_f32_e32 v70, v70
	v_rcp_f32_e32 v82, v82
	v_rcp_f32_e32 v71, v71
	v_rcp_f32_e32 v83, v83
	v_rcp_f32_e32 v72, v72
	v_rcp_f32_e32 v84, v84
	v_rcp_f32_e32 v73, v73
	v_rcp_f32_e32 v85, v85
	v_mul_f32_e32 v47, 0x45800000, v43
	v_mul_f32_e32 v48, 0x45800000, v44
	v_mul_f32_e32 v49, 0x45800000, v45
	v_mul_f32_e32 v11, v11, v42
	v_mul_f32_e32 v13, v13, v42
	v_mul_f32_e32 v12, v12, v42
	v_add_f32_e32 v78, 1.0, v78
	v_add_f32_e32 v90, 1.0, v90
	v_add_f32_e32 v79, 1.0, v79
	v_add_f32_e32 v91, 1.0, v91
	v_add_f32_e32 v80, 1.0, v80
	v_add_f32_e32 v92, 1.0, v92
	v_add_f32_e32 v81, 1.0, v81
	v_add_f32_e32 v93, 1.0, v93
	v_rcp_f32_e32 v74, v74
	v_rcp_f32_e32 v86, v86
	v_rcp_f32_e32 v75, v75
	v_rcp_f32_e32 v87, v87
	v_rcp_f32_e32 v76, v76
	v_rcp_f32_e32 v88, v88
	v_rcp_f32_e32 v77, v77
	v_rcp_f32_e32 v89, v89
	v_cndmask_b32_e32 v43, v43, v47, vcc
	v_cndmask_b32_e64 v44, v44, v48, s[0:1]
	v_cndmask_b32_e64 v45, v45, v49, s[4:5]
	v_mul_f32_e32 v46, v66, v42
	v_mul_f32_e32 v47, v67, v42
	v_mul_f32_e32 v10, v10, v42
	v_mul_f32_e32 v15, v15, v42
	v_mul_f32_e32 v14, v14, v42
	v_mul_f32_e32 v11, v4, v11
	v_mul_f32_e32 v13, v6, v13
	v_mul_f32_e32 v12, v7, v12
	v_rcp_f32_e32 v78, v78
	v_rcp_f32_e32 v90, v90
	v_rcp_f32_e32 v79, v79
	v_rcp_f32_e32 v91, v91
	v_rcp_f32_e32 v80, v80
	v_rcp_f32_e32 v92, v92
	v_rcp_f32_e32 v81, v81
	v_rcp_f32_e32 v93, v93
	v_mul_f32_e32 v42, v94, v43
	v_mul_f32_e32 v48, v95, v43
	v_mul_f32_e32 v17, v17, v43
	v_mul_f32_e32 v16, v16, v43
	v_mul_f32_e32 v19, v19, v43
	v_mul_f32_e32 v18, v18, v43
	v_mul_f32_e32 v21, v21, v43
	v_mul_f32_e32 v20, v20, v43
	v_mul_f32_e32 v43, v102, v44
	v_mul_f32_e32 v49, v103, v44
	v_mul_f32_e32 v23, v23, v44
	v_mul_f32_e32 v22, v22, v44
	v_mul_f32_e32 v25, v25, v44
	v_mul_f32_e32 v24, v24, v44
	v_mul_f32_e32 v31, v31, v44
	v_mul_f32_e32 v30, v30, v44
	v_mul_f32_e32 v44, v104, v45
	v_mul_f32_e32 v50, v105, v45
	v_mul_f32_e32 v37, v37, v45
	v_mul_f32_e32 v36, v36, v45
	v_mul_f32_e32 v39, v39, v45
	v_mul_f32_e32 v38, v38, v45
	v_mul_f32_e32 v41, v41, v45
	v_mul_f32_e32 v40, v40, v45
	v_mul_f32_e32 v45, v2, v46
	v_mul_f32_e32 v46, v3, v47
	v_mul_f32_e32 v10, v5, v10
	v_mul_f32_e32 v15, v8, v15
	v_mul_f32_e32 v14, v9, v14
	v_mul_f32_e32 v11, v98, v11
	v_mul_f32_e32 v13, v68, v13
	v_mul_f32_e32 v12, v100, v12
	v_mul_f32_e32 v42, v2, v42
	v_mul_f32_e32 v47, v3, v48
	v_mul_f32_e32 v17, v4, v17
	v_mul_f32_e32 v16, v5, v16
	v_mul_f32_e32 v19, v6, v19
	v_mul_f32_e32 v18, v7, v18
	v_mul_f32_e32 v21, v8, v21
	v_mul_f32_e32 v20, v9, v20
	v_mul_f32_e32 v48, v3, v49
	v_mul_f32_e32 v49, v3, v50
	v_mul_f32_e32 v45, v96, v45
	v_mul_f32_e32 v46, v97, v46
	v_mul_f32_e32 v50, v99, v10
	v_mul_f32_e32 v15, v69, v15
	v_mul_f32_e32 v14, v101, v14
	v_cvt_pk_bf16_f32 v10, v45, v46
	v_cvt_pk_bf16_f32 v11, v11, v50
	v_cvt_pk_bf16_f32 v12, v13, v12
	v_cvt_pk_bf16_f32 v13, v15, v14
	v_mul_f32_e32 v43, v2, v43
	v_mul_f32_e32 v23, v4, v23
	v_mul_f32_e32 v22, v5, v22
	v_mul_f32_e32 v25, v6, v25
	v_mul_f32_e32 v24, v7, v24
	v_mul_f32_e32 v31, v8, v31
	v_mul_f32_e32 v30, v9, v30
	v_mul_f32_e32 v42, v70, v42
	v_mul_f32_e32 v47, v82, v47
	v_mul_f32_e32 v17, v71, v17
	v_mul_f32_e32 v16, v83, v16
	v_mul_f32_e32 v19, v72, v19
	v_mul_f32_e32 v18, v84, v18
	v_mul_f32_e32 v21, v73, v21
	v_mul_f32_e32 v20, v85, v20
	global_store_dwordx4 v[28:29], v[10:13], off offset:-3072
	v_mul_f32_e32 v44, v2, v44
	v_mul_f32_e32 v37, v4, v37
	v_cvt_pk_bf16_f32 v10, v42, v47
	v_cvt_pk_bf16_f32 v11, v17, v16
	v_cvt_pk_bf16_f32 v12, v19, v18
	v_cvt_pk_bf16_f32 v13, v21, v20
	v_mul_f32_e32 v36, v5, v36
	v_mul_f32_e32 v39, v6, v39
	v_mul_f32_e32 v38, v7, v38
	v_mul_f32_e32 v41, v8, v41
	v_mul_f32_e32 v40, v9, v40
	v_mul_f32_e32 v43, v74, v43
	v_mul_f32_e32 v48, v86, v48
	v_mul_f32_e32 v23, v75, v23
	v_mul_f32_e32 v22, v87, v22
	v_mul_f32_e32 v25, v76, v25
	v_mul_f32_e32 v24, v88, v24
	v_mul_f32_e32 v31, v77, v31
	v_mul_f32_e32 v30, v89, v30
	global_store_dwordx4 v[28:29], v[10:13], off offset:-2048
	v_mul_f32_e32 v44, v78, v44
	v_mul_f32_e32 v49, v90, v49
	v_cvt_pk_bf16_f32 v10, v43, v48
	v_cvt_pk_bf16_f32 v11, v23, v22
	v_cvt_pk_bf16_f32 v12, v25, v24
	v_cvt_pk_bf16_f32 v13, v31, v30
	v_mul_f32_e32 v37, v79, v37
	v_mul_f32_e32 v36, v91, v36
	v_mul_f32_e32 v39, v80, v39
	v_mul_f32_e32 v38, v92, v38
	v_mul_f32_e32 v41, v81, v41
	v_mul_f32_e32 v40, v93, v40
	global_store_dwordx4 v[28:29], v[10:13], off offset:-1024
	s_nop 1
	v_cvt_pk_bf16_f32 v10, v44, v49
	v_cvt_pk_bf16_f32 v11, v37, v36
	v_cvt_pk_bf16_f32 v12, v39, v38
	v_cvt_pk_bf16_f32 v13, v41, v40
	global_store_dwordx4 v[28:29], v[10:13], off
	s_cbranch_scc1 .LBB0_579
